# MoE hook rounds 6-9 split 2/1/1 over the three sub-phases (was 2/2/0)
# speedup vs baseline: 1.0113x; 1.0056x over previous
; __device__ __forceinline__ int moe_t1(int NT, int G) { const int t1 = NT < G / 4 ? NT : G / 4; return (4 * (NT - t1) < G / 2) ? t1 : NT; }
; #define INL(j) (((MK_PHMASK >> (j)) & 1) && INR(pb + (j)))
; #define SEAM(k) do { if (INR(k) && INR((k) + 1)) xcd_barrier(bar); F.lane = lane_id_v(); F.tid = F.wave * 64 + F.lane; { int z_; asm volatile("s_mov_b32 %0, 0" : "=s"(z_)); F.ws = args.ws + z_; F.out = args.out + z_; F.ctl = (gu32*)(args.ws + WS_CTL) + z_; F.in = args.in + z_; F.gw = gw0 + z_; } } while (0)
; __global__ void __launch_bounds__(NTHR, 2) mega_fwd(Args args) {
;     ...
; #pragma unroll 1
;         for (int sp = 0; sp < 3; ++sp) {
;             if (INL(10 + sp)) {
;                 if (sp == 0) moe_tables(F, l);
;                 const int NT = (int)F.MISC[MT_NT], T1 = moe_t1(NT, F.G), nUW = 4 * (NT - T1), nUR = (nUW + 7) & ~7;
;                 const bool doUp = sp == 0 || (sp == 1 && bx < nUW), doDown = (sp == 1 && bx >= nUR) || sp == 2;
;                 if (doUp) {
;                     SchedMoeUp Sc{F.MISC, (const char*)WSP(bf16_t, WS_W13 + l * SZ_W13), (char*)WSP(bf16_t, WS_HMID), WSP(int, WS_LIST), sp == 0 ? 0 : T1, sp == 0 ? 4 * T1 : nUW, bx, sp == 0 ? F.G : nUW};
;                     pg8::EpiSwiGLU E{WSP(float, WS_GATE), WSP(float, WS_RINV)};
;                     pg8::gemm_phase<pg8::EpiSwiGLU, SchedMoeUp, true, true>(F.wave, ring, D, D * 2, D * 2, (const char*)WSP(bf16_t, WS_XB), Sc, E);
;                 }
;                 if (doDown) {
;                     SchedMoeDown Sc{F.MISC, (const char*)WSP(bf16_t, WS_HMID), (const char*)WSP(bf16_t, WS_W2 + l * SZ_W2), (char*)WSP(bf16_t, WS_Y), sp == 1 ? 0 : T1, sp == 1 ? 8 * T1 : 8 * (NT - T1), sp == 1 ? bx - nUR : bx, sp == 1 ? F.G - nUR : F.G};
;                     pg8::EpiBf16 E{nullptr, 0};
;                     pg8::gemm_phase<pg8::EpiBf16, SchedMoeDown, false, false>(F.wave, ring, FH, FH * 2, FH * 2, nullptr, Sc, E);
;                 }
;             }
;             SEAM(pb + 10 + sp);
;         }
.LBB0_1552:
	v_readlane_b32 s100, v251, 3
	s_nop 3
	s_bitcmp1_b32 s100, 3
	s_cbranch_scc1 .Lcv_ret_9
	s_add_i32 s100, s87, 8
	s_nop 0
	s_min_u32 s100, s100, 10
	s_cmp_ge_u32 s101, s100
	s_cbranch_scc1 .Lcv_ret_9
	s_lshl_b32 s100, s100, 8
	s_or_b32 s100, s100, 9
	s_branch .Lcv_run

; __device__ __forceinline__ int moe_t1(int NT, int G) { const int t1 = NT < G / 4 ? NT : G / 4; return (4 * (NT - t1) < G / 2) ? t1 : NT; }
; #define INL(j) (((MK_PHMASK >> (j)) & 1) && INR(pb + (j)))
; #define SEAM(k) do { if (INR(k) && INR((k) + 1)) xcd_barrier(bar); F.lane = lane_id_v(); F.tid = F.wave * 64 + F.lane; { int z_; asm volatile("s_mov_b32 %0, 0" : "=s"(z_)); F.ws = args.ws + z_; F.out = args.out + z_; F.ctl = (gu32*)(args.ws + WS_CTL) + z_; F.in = args.in + z_; F.gw = gw0 + z_; } } while (0)
; __global__ void __launch_bounds__(NTHR, 2) mega_fwd(Args args) {
;     ...
; #pragma unroll 1
;         for (int sp = 0; sp < 3; ++sp) {
;             if (INL(10 + sp)) {
;                 if (sp == 0) moe_tables(F, l);
;                 const int NT = (int)F.MISC[MT_NT], T1 = moe_t1(NT, F.G), nUW = 4 * (NT - T1), nUR = (nUW + 7) & ~7;
;                 const bool doUp = sp == 0 || (sp == 1 && bx < nUW), doDown = (sp == 1 && bx >= nUR) || sp == 2;
;                 if (doUp) {
;                     SchedMoeUp Sc{F.MISC, (const char*)WSP(bf16_t, WS_W13 + l * SZ_W13), (char*)WSP(bf16_t, WS_HMID), WSP(int, WS_LIST), sp == 0 ? 0 : T1, sp == 0 ? 4 * T1 : nUW, bx, sp == 0 ? F.G : nUW};
;                     pg8::EpiSwiGLU E{WSP(float, WS_GATE), WSP(float, WS_RINV)};
;                     pg8::gemm_phase<pg8::EpiSwiGLU, SchedMoeUp, true, true>(F.wave, ring, D, D * 2, D * 2, (const char*)WSP(bf16_t, WS_XB), Sc, E);
;                 }
;                 if (doDown) {
;                     SchedMoeDown Sc{F.MISC, (const char*)WSP(bf16_t, WS_HMID), (const char*)WSP(bf16_t, WS_W2 + l * SZ_W2), (char*)WSP(bf16_t, WS_Y), sp == 1 ? 0 : T1, sp == 1 ? 8 * T1 : 8 * (NT - T1), sp == 1 ? bx - nUR : bx, sp == 1 ? F.G - nUR : F.G};
;                     pg8::EpiBf16 E{nullptr, 0};
;                     pg8::gemm_phase<pg8::EpiBf16, SchedMoeDown, false, false>(F.wave, ring, FH, FH * 2, FH * 2, nullptr, Sc, E);
;                 }
;             }
;             SEAM(pb + 10 + sp);
;         }
.LBB0_1642:
	s_add_i32 s94, s94, 1
	s_cmp_lt_i32 s94, s75
	s_cselect_b64 s[4:5], -1, 0
	s_and_b64 s[4:5], s[70:71], s[4:5]
	s_andn2_b64 vcc, exec, s[4:5]
	s_cbranch_vccnz .LBB0_1551
	v_readlane_b32 s100, v251, 3
	s_nop 3
	s_bitcmp1_b32 s100, 3
	s_cbranch_scc0 .Lcv_ret_11
	s_add_i32 s100, s87, 8
	s_nop 0
	s_min_u32 s100, s100, 10
	s_cmp_ge_u32 s101, s100
	s_cbranch_scc1 .Lcv_ret_11
	s_lshl_b32 s100, s100, 8
	s_or_b32 s100, s100, 11
	s_branch .Lcv_run
